# speedup vs baseline: 1.0033x; 1.0033x over previous
.Lmy_ffn3_k1:
	ds_read_b128 v[32:35], v156
	ds_read_b128 v[36:39], v156 offset:32
	ds_read_b128 v[40:43], v156 offset:64
	ds_read_b128 v[44:47], v156 offset:96
	ds_read_b128 v[140:143], v101
	ds_read_b128 v[144:147], v101 offset:1024
	ds_read_b128 v[148:151], v101 offset:2048
	ds_read_b128 v[152:155], v101 offset:3072
	v_add_u32_e32 v101, 0x1000, v101
	v_add_u32_e32 v156, 0x80, v156
	s_add_i32 s2, s2, -1
	s_waitcnt lgkmcnt(3)
	v_mfma_f32_32x32x16_f16 v[32:47], v[140:143], v[48:51], v[32:47]
	s_waitcnt lgkmcnt(2)
	v_mfma_f32_32x32x16_f16 v[32:47], v[144:147], v[52:55], v[32:47]
	s_waitcnt lgkmcnt(1)
	v_mfma_f32_32x32x16_f16 v[32:47], v[148:151], v[56:59], v[32:47]
	s_waitcnt lgkmcnt(0)
	v_mfma_f32_32x32x16_f16 v[32:47], v[152:155], v[60:63], v[32:47]
	ds_read_b128 v[112:115], v102
	ds_read_b128 v[116:119], v102 offset:16384
	ds_read_b128 v[104:107], v102 offset:1024
	ds_read_b128 v[120:123], v102 offset:17408
	v_add_u32_e32 v102, 0x800, v102
	s_cmp_lg_u32 s2, 0
	s_nop 5
	v_max_f32_e32 v32, 0, v32
	v_max_f32_e32 v33, 0, v33
	v_max_f32_e32 v34, 0, v34
	v_max_f32_e32 v35, 0, v35
	v_max_f32_e32 v36, 0, v36
	v_max_f32_e32 v37, 0, v37
	v_max_f32_e32 v38, 0, v38
	v_max_f32_e32 v39, 0, v39
	v_cvt_pkrtz_f16_f32 v32, v32, v33
	v_cvt_pkrtz_f16_f32 v33, v34, v35
	v_cvt_pkrtz_f16_f32 v34, v36, v37
	v_cvt_pkrtz_f16_f32 v35, v38, v39
	s_waitcnt lgkmcnt(2)
	s_nop 0
	v_mfma_f32_32x32x16_f16 v[16:31], v[112:115], v[32:35], v[16:31]
	v_mfma_f32_32x32x16_f16 v[0:15], v[116:119], v[32:35], v[0:15]
	v_max_f32_e32 v40, 0, v40
	v_max_f32_e32 v41, 0, v41
	v_max_f32_e32 v42, 0, v42
	v_max_f32_e32 v43, 0, v43
	v_max_f32_e32 v44, 0, v44
	v_max_f32_e32 v45, 0, v45
	v_max_f32_e32 v46, 0, v46
	v_max_f32_e32 v47, 0, v47
	v_cvt_pkrtz_f16_f32 v32, v40, v41
	v_cvt_pkrtz_f16_f32 v33, v42, v43
	v_cvt_pkrtz_f16_f32 v34, v44, v45
	v_cvt_pkrtz_f16_f32 v35, v46, v47
	s_waitcnt lgkmcnt(0)
	s_nop 0
	v_mfma_f32_32x32x16_f16 v[16:31], v[104:107], v[32:35], v[16:31]
	v_mfma_f32_32x32x16_f16 v[0:15], v[120:123], v[32:35], v[0:15]
	s_cbranch_scc1 .Lmy_ffn3_k1
	s_waitcnt lgkmcnt(7)
	s_nop 0
	s_nop 7
	v_pk_add_f32 v[16:17], v[86:87], v[16:17]
	v_pk_add_f32 v[18:19], v[84:85], v[18:19]
	v_add_f32_e32 v48, 0, v16
	v_add_f32_e32 v48, v17, v48
	v_add_f32_e32 v48, v18, v48
	s_waitcnt lgkmcnt(6)
	v_add_f32_e32 v48, v19, v48
	v_pk_add_f32 v[20:21], v[82:83], v[20:21]
	v_add_f32_e32 v48, v20, v48
	v_add_f32_e32 v48, v21, v48
	v_pk_add_f32 v[22:23], v[80:81], v[22:23]
	s_waitcnt lgkmcnt(3)
	v_add_f32_e32 v48, v22, v48
	v_add_f32_e32 v48, v23, v48
	v_pk_add_f32 v[24:25], v[78:79], v[24:25]
	v_add_f32_e32 v48, v24, v48
	v_add_f32_e32 v48, v25, v48
	v_pk_add_f32 v[26:27], v[76:77], v[26:27]
	s_waitcnt lgkmcnt(2)
	v_add_f32_e32 v48, v26, v48
	v_add_f32_e32 v48, v27, v48
	v_pk_add_f32 v[28:29], v[74:75], v[28:29]
	v_add_f32_e32 v48, v28, v48
	v_add_f32_e32 v48, v29, v48
	v_pk_add_f32 v[30:31], v[72:73], v[30:31]
	v_add_f32_e32 v48, v30, v48
	v_add_f32_e32 v48, v31, v48
	v_pk_add_f32 v[0:1], v[70:71], v[0:1]
	v_add_f32_e32 v48, v0, v48
	v_add_f32_e32 v48, v1, v48
	v_pk_add_f32 v[2:3], v[68:69], v[2:3]
	v_add_f32_e32 v48, v2, v48
	v_add_f32_e32 v48, v3, v48
	v_pk_add_f32 v[4:5], v[66:67], v[4:5]
	v_add_f32_e32 v48, v4, v48
	v_pk_add_f32 v[6:7], v[96:97], v[6:7]
	v_add_f32_e32 v48, v5, v48
	s_waitcnt lgkmcnt(1)
	v_add_f32_e32 v48, v6, v48
	v_pk_add_f32 v[8:9], v[88:89], v[8:9]
	v_add_f32_e32 v48, v7, v48
	v_add_f32_e32 v48, v8, v48
	v_pk_add_f32 v[10:11], v[90:91], v[10:11]
	v_add_f32_e32 v48, v9, v48
	s_waitcnt lgkmcnt(0)
	v_add_f32_e32 v48, v10, v48
	v_pk_add_f32 v[12:13], v[92:93], v[12:13]
	v_add_f32_e32 v48, v11, v48
	v_add_f32_e32 v48, v12, v48
	v_pk_add_f32 v[14:15], v[94:95], v[14:15]
	v_add_f32_e32 v48, v13, v48
	v_add_f32_e32 v48, v14, v48
	v_add_f32_e32 v48, v15, v48
	v_mov_b32_e32 v49, v48
	v_mov_b32_e32 v50, v48
	s_nop 1
	v_permlane32_swap_b32_e32 v49, v50
	v_cndmask_b32_e32 v49, v49, v50, vcc
	v_add_f32_e32 v48, v48, v49
	v_mul_f32_e32 v48, 0x3c800000, v48
	v_pk_add_f32 v[16:17], v[16:17], v[48:49] op_sel_hi:[1,0] neg_lo:[0,1] neg_hi:[0,1]
	v_pk_add_f32 v[18:19], v[18:19], v[48:49] op_sel_hi:[1,0] neg_lo:[0,1] neg_hi:[0,1]
	v_pk_mul_f32 v[50:51], v[16:17], v[16:17]
	v_pk_mul_f32 v[52:53], v[18:19], v[18:19]
	v_add_f32_e32 v50, v50, v51
	v_pk_add_f32 v[20:21], v[20:21], v[48:49] op_sel_hi:[1,0] neg_lo:[0,1] neg_hi:[0,1]
	v_add_f32_e32 v50, v52, v50
	v_pk_mul_f32 v[54:55], v[20:21], v[20:21]
	v_add_f32_e32 v50, v53, v50
	v_pk_add_f32 v[22:23], v[22:23], v[48:49] op_sel_hi:[1,0] neg_lo:[0,1] neg_hi:[0,1]
	v_add_f32_e32 v50, v54, v50
	v_pk_mul_f32 v[56:57], v[22:23], v[22:23]
	v_add_f32_e32 v50, v55, v50
	v_pk_add_f32 v[24:25], v[24:25], v[48:49] op_sel_hi:[1,0] neg_lo:[0,1] neg_hi:[0,1]
	v_add_f32_e32 v50, v56, v50
	v_pk_mul_f32 v[58:59], v[24:25], v[24:25]
	v_add_f32_e32 v50, v57, v50
	v_pk_add_f32 v[26:27], v[26:27], v[48:49] op_sel_hi:[1,0] neg_lo:[0,1] neg_hi:[0,1]
	v_add_f32_e32 v50, v58, v50
	v_pk_mul_f32 v[60:61], v[26:27], v[26:27]
	v_add_f32_e32 v50, v59, v50
	v_pk_add_f32 v[28:29], v[28:29], v[48:49] op_sel_hi:[1,0] neg_lo:[0,1] neg_hi:[0,1]
	v_add_f32_e32 v50, v60, v50
	v_lshlrev_b64 v[62:63], 7, v[64:65]
	v_pk_mul_f32 v[64:65], v[28:29], v[28:29]
	v_add_f32_e32 v50, v61, v50
	v_pk_add_f32 v[30:31], v[30:31], v[48:49] op_sel_hi:[1,0] neg_lo:[0,1] neg_hi:[0,1]
	v_add_f32_e32 v50, v64, v50
	v_pk_mul_f32 v[66:67], v[30:31], v[30:31]
	v_add_f32_e32 v50, v65, v50
	v_pk_add_f32 v[0:1], v[0:1], v[48:49] op_sel_hi:[1,0] neg_lo:[0,1] neg_hi:[0,1]
	v_add_f32_e32 v50, v66, v50
	v_pk_mul_f32 v[68:69], v[0:1], v[0:1]
	v_add_f32_e32 v50, v67, v50
	v_pk_add_f32 v[2:3], v[2:3], v[48:49] op_sel_hi:[1,0] neg_lo:[0,1] neg_hi:[0,1]
	v_add_f32_e32 v50, v68, v50
	v_pk_mul_f32 v[70:71], v[2:3], v[2:3]
	v_add_f32_e32 v50, v69, v50
	v_pk_add_f32 v[4:5], v[4:5], v[48:49] op_sel_hi:[1,0] neg_lo:[0,1] neg_hi:[0,1]
	v_add_f32_e32 v50, v70, v50
	v_pk_mul_f32 v[72:73], v[4:5], v[4:5]
	v_add_f32_e32 v50, v71, v50
	v_pk_add_f32 v[6:7], v[6:7], v[48:49] op_sel_hi:[1,0] neg_lo:[0,1] neg_hi:[0,1]
	v_add_f32_e32 v50, v72, v50
	v_pk_add_f32 v[8:9], v[8:9], v[48:49] op_sel_hi:[1,0] neg_lo:[0,1] neg_hi:[0,1]
	v_pk_add_f32 v[10:11], v[10:11], v[48:49] op_sel_hi:[1,0] neg_lo:[0,1] neg_hi:[0,1]
	v_pk_add_f32 v[12:13], v[12:13], v[48:49] op_sel_hi:[1,0] neg_lo:[0,1] neg_hi:[0,1]
	v_pk_add_f32 v[14:15], v[14:15], v[48:49] op_sel_hi:[1,0] neg_lo:[0,1] neg_hi:[0,1]
	v_pk_mul_f32 v[48:49], v[6:7], v[6:7]
	v_add_f32_e32 v50, v73, v50
	v_add_f32_e32 v48, v48, v50
	v_pk_mul_f32 v[74:75], v[8:9], v[8:9]
	v_add_f32_e32 v48, v49, v48
	v_add_f32_e32 v48, v74, v48
	v_pk_mul_f32 v[76:77], v[10:11], v[10:11]
	v_add_f32_e32 v48, v75, v48
	v_add_f32_e32 v48, v76, v48
	v_pk_mul_f32 v[78:79], v[12:13], v[12:13]
	v_add_f32_e32 v48, v77, v48
	v_add_f32_e32 v48, v78, v48
	v_pk_mul_f32 v[80:81], v[14:15], v[14:15]
	v_add_f32_e32 v48, v79, v48
	v_add_f32_e32 v48, v80, v48
	v_add_f32_e32 v48, v81, v48
	v_mov_b32_e32 v49, v48
	v_mov_b32_e32 v50, v48
	s_nop 1
	v_permlane32_swap_b32_e32 v49, v50
	v_cndmask_b32_e32 v49, v49, v50, vcc
	v_add_f32_e32 v48, v48, v49
	v_mov_b32_e32 v49, 0x3727c5ac
	v_fmac_f32_e32 v49, 0x3c800000, v48
	v_rsq_f32_e32 v48, v49
	ds_read_b128 v[118:121], v99 offset:3648
	ds_read_b128 v[122:125], v99 offset:3680
	ds_read_b128 v[126:129], v99 offset:3904
	ds_read_b128 v[130:133], v99 offset:3936
	ds_read_b128 v[134:137], v99 offset:3712
	ds_read_b128 v[138:141], v99 offset:3744
	ds_read_b128 v[142:145], v99 offset:3968
	ds_read_b128 v[146:149], v99 offset:4000
	ds_read_b128 v[150:153], v99 offset:3776
	ds_read_b128 v[154:157], v99 offset:3808
	ds_read_b128 v[158:161], v99 offset:4032
	ds_read_b128 v[162:165], v99 offset:4064
	ds_read_b128 v[40:43], v99 offset:3840
	ds_read_b128 v[32:35], v99 offset:3872
	ds_read_b128 v[44:47], v99 offset:4096
	ds_read_b128 v[36:39], v99 offset:4128
	v_lshl_add_u64 v[62:63], s[0:1], 0, v[62:63]
	v_lshlrev_b32_e32 v50, 1, v100
	v_pk_mul_f32 v[0:1], v[0:1], v[48:49] op_sel_hi:[1,0]
	v_pk_mul_f32 v[2:3], v[2:3], v[48:49] op_sel_hi:[1,0]
	v_mov_b32_e32 v51, 0
	s_waitcnt lgkmcnt(5)
	v_pk_fma_f32 v[0:1], v[150:151], v[0:1], v[158:159]
	v_pk_fma_f32 v[2:3], v[152:153], v[2:3], v[160:161]
	v_pk_mul_f32 v[4:5], v[4:5], v[48:49] op_sel_hi:[1,0]
	v_pk_mul_f32 v[6:7], v[6:7], v[48:49] op_sel_hi:[1,0]
	v_lshl_add_u64 v[50:51], v[62:63], 0, v[50:51]
	v_mbcnt_lo_u32_b32 v218, -1, 0
	v_mbcnt_hi_u32_b32 v218, -1, v218
	v_and_b32_e32 v218, 32, v218
	v_lshrrev_b32_e32 v218, 2, v218
	v_mov_b32_e32 v219, 0
	v_lshl_add_u64 v[216:217], v[50:51], 0, v[218:219]
	s_waitcnt lgkmcnt(4)
	v_pk_fma_f32 v[4:5], v[154:155], v[4:5], v[162:163]
	v_pk_fma_f32 v[6:7], v[156:157], v[6:7], v[164:165]
	v_cvt_pk_f16_f32 v208, v0, v1
	v_cvt_pk_f16_f32 v209, v2, v3
	v_cvt_pk_f16_f32 v210, v4, v5
	v_cvt_pk_f16_f32 v211, v6, v7
	v_pk_mul_f32 v[16:17], v[16:17], v[48:49] op_sel_hi:[1,0]
	v_pk_mul_f32 v[18:19], v[18:19], v[48:49] op_sel_hi:[1,0]
	s_nop 1
	v_permlane32_swap_b32_e32 v208, v210
	v_permlane32_swap_b32_e32 v209, v211
	global_store_dwordx4 v[216:217], v[208:211], off offset:64
	v_pk_mul_f32 v[0:1], v[8:9], v[48:49] op_sel_hi:[1,0]
	v_pk_mul_f32 v[2:3], v[10:11], v[48:49] op_sel_hi:[1,0]
	v_pk_fma_f32 v[16:17], v[118:119], v[16:17], v[126:127]
	v_pk_fma_f32 v[18:19], v[120:121], v[18:19], v[128:129]
	v_pk_mul_f32 v[20:21], v[20:21], v[48:49] op_sel_hi:[1,0]
	v_pk_mul_f32 v[22:23], v[22:23], v[48:49] op_sel_hi:[1,0]
	s_waitcnt lgkmcnt(1)
	v_pk_fma_f32 v[0:1], v[40:41], v[0:1], v[44:45]
	v_pk_fma_f32 v[2:3], v[42:43], v[2:3], v[46:47]
	v_pk_fma_f32 v[20:21], v[122:123], v[20:21], v[130:131]
	v_pk_fma_f32 v[22:23], v[124:125], v[22:23], v[132:133]
	v_pk_mul_f32 v[24:25], v[24:25], v[48:49] op_sel_hi:[1,0]
	v_pk_mul_f32 v[26:27], v[26:27], v[48:49] op_sel_hi:[1,0]
	v_cvt_pk_f16_f32 v200, v16, v17
	v_cvt_pk_f16_f32 v201, v18, v19
	v_cvt_pk_f16_f32 v212, v0, v1
	v_cvt_pk_f16_f32 v213, v2, v3
	v_pk_fma_f32 v[24:25], v[134:135], v[24:25], v[142:143]
	v_pk_fma_f32 v[26:27], v[136:137], v[26:27], v[144:145]
	v_pk_mul_f32 v[28:29], v[28:29], v[48:49] op_sel_hi:[1,0]
	v_pk_mul_f32 v[30:31], v[30:31], v[48:49] op_sel_hi:[1,0]
	v_cvt_pk_f16_f32 v202, v20, v21
	v_cvt_pk_f16_f32 v203, v22, v23
	v_pk_mul_f32 v[0:1], v[12:13], v[48:49] op_sel_hi:[1,0]
	v_pk_mul_f32 v[2:3], v[14:15], v[48:49] op_sel_hi:[1,0]
	v_pk_fma_f32 v[28:29], v[138:139], v[28:29], v[146:147]
	v_pk_fma_f32 v[30:31], v[140:141], v[30:31], v[148:149]
	v_permlane32_swap_b32_e32 v200, v202
	v_permlane32_swap_b32_e32 v201, v203
	global_store_dwordx4 v[216:217], v[200:203], off
	v_cvt_pk_f16_f32 v204, v24, v25
	v_cvt_pk_f16_f32 v205, v26, v27
	s_waitcnt lgkmcnt(0)
	v_pk_fma_f32 v[0:1], v[32:33], v[0:1], v[36:37]
	v_pk_fma_f32 v[2:3], v[34:35], v[2:3], v[38:39]
	v_cvt_pk_f16_f32 v206, v28, v29
	v_cvt_pk_f16_f32 v207, v30, v31
	v_cvt_pk_f16_f32 v214, v0, v1
	v_cvt_pk_f16_f32 v215, v2, v3
	s_nop 1
	v_permlane32_swap_b32_e32 v204, v206
	v_permlane32_swap_b32_e32 v205, v207
	v_permlane32_swap_b32_e32 v212, v214
	v_permlane32_swap_b32_e32 v213, v215
	global_store_dwordx4 v[216:217], v[204:207], off offset:32
	global_store_dwordx4 v[216:217], v[212:215], off offset:96
	s_endpgm
